# v24_btswz
# speedup vs baseline: 1.0233x; 1.0060x over previous
.LBB4_4:
	s_or_b64 exec, exec, s[4:5]
	s_waitcnt vmcnt(0)
	ds_write_b32 v247, v246
	v_and_b32_e32 v62, 24, v62
	v_lshrrev_b32_e32 v200, 2, v0
	v_lshlrev_b32_e32 v201, 1, v62
	v_lshrrev_b32_e32 v246, 1, v0
	v_xor_b32_e32 v246, v246, v0
	v_and_b32_e32 v246, 16, v246
	v_xor_b32_e32 v201, v201, v246
	s_movk_i32 s4, 0x50
	v_mad_u32_u24 v62, v200, s4, v201
	v_add_u32_e32 v63, 0xa000, v62
	ds_write_b128 v62, v[10:13] offset:40960
	ds_write_b128 v62, v[14:17] offset:51200
	ds_write_b128 v62, v[58:61] offset:61440
	ds_write_b128 v63, v[34:37] offset:30720
	s_and_saveexec_b64 s[4:5], s[2:3]
	s_cbranch_execz .LBB4_6
	v_mul_u32_u24_e32 v10, 0x90, v1
	v_and_b32_e32 v11, 0x70, v210
	s_mov_b32 s10, 0x19a00
	v_add3_u32 v10, v10, v11, s10
	s_waitcnt vmcnt(0)
	ds_write_b128 v10, v[2:5]

.LBB4_10:
	s_or_b64 exec, exec, s[12:13]
	global_load_dwordx4 v[10:13], v[216:217], off offset:1424 nt
	global_load_dwordx4 v[14:17], v[216:217], off offset:1408 nt
	v_lshlrev_b32_e32 v79, 2, v198
	v_lshl_or_b32 v212, v78, 9, v79
	v_mul_u32_u24_e32 v78, 36, v80
	v_lshlrev_b32_e32 v98, 2, v78
	v_lshlrev_b32_e32 v99, 2, v211
	s_mov_b32 s13, 0x18800
	v_add3_u32 v218, v98, v99, s13
	ds_read_b128 v[82:85], v218 offset:6912
	ds_read_b128 v[86:89], v218 offset:6928
	v_mul_f32_e32 v199, v75, v75
	v_fmac_f32_e32 v199, v74, v74
	v_mul_u32_u24_e32 v219, 40, v80
	v_lshlrev_b32_e32 v78, 1, v211
	v_lshrrev_b32_e32 v247, 1, v80
	v_xor_b32_e32 v247, v247, v80
	v_and_b32_e32 v247, 4, v247
	v_lshlrev_b32_e32 v247, 2, v247
	v_xor_b32_e32 v78, v78, v247
	v_fmac_f32_e32 v199, v76, v76
	v_lshl_add_u32 v222, v219, 1, v78
	v_fmac_f32_e32 v199, v77, v77
	s_waitcnt lgkmcnt(1)
	v_pk_add_f32 v[76:77], v[76:77], v[84:85]
	v_pk_add_f32 v[74:75], v[74:75], v[82:83]
	ds_read_b128 v[78:81], v222 offset:40960
	ds_read_b128 v[82:85], v222 offset:42240
	s_waitcnt lgkmcnt(2)
	v_pk_add_f32 v[92:93], v[72:73], v[88:89]
	v_pk_add_f32 v[90:91], v[70:71], v[86:87]
	ds_read_b128 v[86:89], v222 offset:43520
	ds_read_b128 v[94:97], v222 offset:44800
	s_mul_i32 s12, s18, 0x900
	s_add_i32 s12, s12, 0x14000
	v_add_u32_e32 v213, s12, v98
	v_cvt_pk_f16_f32 v205, v92, v93
	v_cvt_pk_f16_f32 v203, v76, v77
	v_cvt_pk_f16_f32 v204, v90, v91
	v_cvt_pk_f16_f32 v202, v74, v75
	v_add_u32_e32 v220, v213, v99
	v_fmac_f32_e32 v199, v70, v70
	s_waitcnt lgkmcnt(3)
	v_mfma_f32_16x16x32_f16 v[78:81], v[78:81], v[202:205], 0
	ds_write_b128 v220, v[74:77]
	ds_write_b128 v220, v[90:93] offset:16
	v_fmac_f32_e32 v199, v71, v71
	v_fmac_f32_e32 v199, v72, v72
	s_waitcnt lgkmcnt(4)
	v_mfma_f32_16x16x32_f16 v[82:85], v[82:85], v[202:205], 0
	v_fmac_f32_e32 v199, v73, v73
	s_waitcnt lgkmcnt(3)
	v_mfma_f32_16x16x32_f16 v[86:89], v[86:89], v[202:205], 0
	s_waitcnt lgkmcnt(2)
	v_mfma_f32_16x16x32_f16 v[90:93], v[94:97], v[202:205], 0
	ds_read_b128 v[70:73], v222 offset:46080
	ds_read_b128 v[74:77], v222 offset:47360
	s_waitcnt lgkmcnt(1)
	v_mfma_f32_16x16x32_f16 v[94:97], v[70:73], v[202:205], 0
	ds_read_b128 v[70:73], v222 offset:48640
	s_waitcnt lgkmcnt(1)
	v_mfma_f32_16x16x32_f16 v[98:101], v[74:77], v[202:205], 0
	ds_read_b128 v[74:77], v222 offset:49920
	s_waitcnt lgkmcnt(1)
	v_mfma_f32_16x16x32_f16 v[102:105], v[70:73], v[202:205], 0
	s_waitcnt lgkmcnt(0)
	v_mfma_f32_16x16x32_f16 v[106:109], v[74:77], v[202:205], 0
	ds_read_b128 v[70:73], v222 offset:51200
	ds_read_b128 v[74:77], v222 offset:52480
	s_waitcnt lgkmcnt(1)
	v_mfma_f32_16x16x32_f16 v[110:113], v[70:73], v[202:205], 0
	ds_read_b128 v[70:73], v222 offset:53760
	s_waitcnt lgkmcnt(1)
	v_mfma_f32_16x16x32_f16 v[114:117], v[74:77], v[202:205], 0
	ds_read_b128 v[74:77], v222 offset:55040
	s_waitcnt lgkmcnt(1)
	v_mfma_f32_16x16x32_f16 v[118:121], v[70:73], v[202:205], 0
	s_waitcnt lgkmcnt(0)
	v_mfma_f32_16x16x32_f16 v[122:125], v[74:77], v[202:205], 0
	ds_read_b128 v[70:73], v222 offset:56320
	ds_read_b128 v[74:77], v222 offset:57600
	s_waitcnt lgkmcnt(1)
	v_mfma_f32_16x16x32_f16 v[126:129], v[70:73], v[202:205], 0
	ds_read_b128 v[70:73], v222 offset:58880
	s_waitcnt lgkmcnt(1)
	v_mfma_f32_16x16x32_f16 v[130:133], v[74:77], v[202:205], 0
	ds_read_b128 v[74:77], v222 offset:60160
	s_waitcnt lgkmcnt(1)
	v_mfma_f32_16x16x32_f16 v[134:137], v[70:73], v[202:205], 0
	s_waitcnt lgkmcnt(0)
	v_mfma_f32_16x16x32_f16 v[138:141], v[74:77], v[202:205], 0
	ds_read_b128 v[70:73], v222 offset:61440
	ds_read_b128 v[74:77], v222 offset:62720
	s_waitcnt lgkmcnt(1)
	v_mfma_f32_16x16x32_f16 v[142:145], v[70:73], v[202:205], 0
	ds_read_b128 v[70:73], v222 offset:64000
	s_waitcnt lgkmcnt(1)
	v_mfma_f32_16x16x32_f16 v[146:149], v[74:77], v[202:205], 0
	ds_read_b128 v[74:77], v222 offset:65280
	s_waitcnt lgkmcnt(1)
	v_mfma_f32_16x16x32_f16 v[150:153], v[70:73], v[202:205], 0
	s_waitcnt lgkmcnt(0)
	v_mfma_f32_16x16x32_f16 v[154:157], v[74:77], v[202:205], 0
	v_add_u32_e32 v70, 0x10400, v222
	ds_read_b128 v[70:73], v70
	v_add_u32_e32 v74, 0x10900, v222
	ds_read_b128 v[74:77], v74
	v_add_u32_e32 v162, 0x10e00, v222
	s_waitcnt lgkmcnt(1)
	v_mfma_f32_16x16x32_f16 v[158:161], v[70:73], v[202:205], 0
	ds_read_b128 v[70:73], v162
	v_add_u32_e32 v162, 0x11300, v222
	s_waitcnt lgkmcnt(1)
	v_mfma_f32_16x16x32_f16 v[170:173], v[74:77], v[202:205], 0
	ds_read_b128 v[74:77], v162
	s_waitcnt lgkmcnt(1)
	v_mfma_f32_16x16x32_f16 v[162:165], v[70:73], v[202:205], 0
	s_waitcnt lgkmcnt(0)
	v_mfma_f32_16x16x32_f16 v[166:169], v[74:77], v[202:205], 0
	v_add_u32_e32 v226, 0x11800, v222
	ds_read_b128 v[70:73], v226
	v_add_u32_e32 v74, 0x11d00, v222
	ds_read_b128 v[74:77], v74
	v_add_u32_e32 v178, 0x12200, v222
	s_waitcnt lgkmcnt(1)
	v_mfma_f32_16x16x32_f16 v[174:177], v[70:73], v[202:205], 0
	ds_read_b128 v[70:73], v178
	v_add_u32_e32 v178, 0x12700, v222
	s_waitcnt lgkmcnt(1)
	v_mfma_f32_16x16x32_f16 v[186:189], v[74:77], v[202:205], 0
	ds_read_b128 v[74:77], v178
	s_waitcnt lgkmcnt(1)
	v_mfma_f32_16x16x32_f16 v[178:181], v[70:73], v[202:205], 0
	s_waitcnt lgkmcnt(0)
	v_mfma_f32_16x16x32_f16 v[182:185], v[74:77], v[202:205], 0
	v_add_u32_e32 v70, 0x12c00, v222
	v_add_u32_e32 v74, 0x13100, v222
	ds_read_b128 v[70:73], v70
	ds_read_b128 v[74:77], v74
	v_add_u32_e32 v194, 0x13600, v222
	v_add_u32_e32 v206, 0x13b00, v222
	s_waitcnt lgkmcnt(1)
	v_mfma_f32_16x16x32_f16 v[190:193], v[70:73], v[202:205], 0
	ds_read_b128 v[70:73], v194
	s_waitcnt lgkmcnt(1)
	v_mfma_f32_16x16x32_f16 v[194:197], v[74:77], v[202:205], 0
	ds_read_b128 v[74:77], v206
	s_waitcnt lgkmcnt(1)
	v_mfma_f32_16x16x32_f16 v[206:209], v[70:73], v[202:205], 0
	s_waitcnt lgkmcnt(0)
	v_mfma_f32_16x16x32_f16 v[72:75], v[74:77], v[202:205], 0
	v_lshlrev_b32_e32 v70, 4, v198
	v_or_b32_e32 v71, 0x1b380, v70
	v_add_u32_e32 v221, v213, v70
	ds_read_b128 v[202:205], v71
	ds_read_b128 v[228:231], v221
	v_or_b32_e32 v71, 0x1b3c0, v70
	ds_read_b128 v[232:235], v71
	ds_read_b128 v[236:239], v221 offset:64
	s_mov_b32 s12, 0x39800000
	v_mov_b32_e32 v213, 0
	s_waitcnt lgkmcnt(2)
	v_pk_mul_f32 v[202:203], v[202:203], v[228:229]
	v_pk_mul_f32 v[76:77], v[204:205], v[230:231]
	v_pk_fma_f32 v[202:203], v[206:207], s[12:13], v[202:203] op_sel_hi:[1,0,1]
	v_pk_fma_f32 v[204:205], v[208:209], s[12:13], v[76:77] op_sel_hi:[1,0,1]
	v_pk_mul_f32 v[206:207], v[202:203], v[202:203]
	v_lshl_add_u64 v[212:213], v[212:213], 2, s[10:11]
	v_pk_mul_f32 v[76:77], v[204:205], v[204:205]
	global_store_dwordx4 v[212:213], v[202:205], off offset:1920 nt
	v_add_f32_e32 v71, v207, v206
	v_add_f32_e32 v71, v76, v71
	s_waitcnt lgkmcnt(0)
	v_pk_mul_f32 v[204:205], v[232:233], v[236:237]
	v_pk_mul_f32 v[202:203], v[234:235], v[238:239]
	v_pk_fma_f32 v[72:73], v[72:73], s[12:13], v[204:205] op_sel_hi:[1,0,1]
	v_add_f32_e32 v71, v77, v71
	v_pk_mul_f32 v[204:205], v[72:73], v[72:73]
	v_pk_fma_f32 v[74:75], v[74:75], s[12:13], v[202:203] op_sel_hi:[1,0,1]
	v_add_f32_e32 v71, v71, v204
	v_pk_mul_f32 v[202:203], v[74:75], v[74:75]
	v_add_f32_e32 v71, v205, v71
	v_add_f32_e32 v71, v202, v71
	v_add_f32_e32 v228, v203, v71
	v_mul_u32_u24_e32 v71, 40, v200
	v_lshl_add_u32 v224, v71, 1, v201
	global_store_dwordx4 v[212:213], v[72:75], off offset:1984 nt
	ds_write_b128 v224, v[6:9]
	ds_write_b128 v224, v[22:25] offset:10240
	ds_write_b128 v224, v[30:33] offset:20480
	s_and_saveexec_b64 s[10:11], s[6:7]
	ds_write_b128 v224, v[42:45] offset:30720
	s_or_b64 exec, exec, s[10:11]
	s_and_saveexec_b64 s[10:11], s[2:3]
	s_cbranch_execz .LBB4_14
	v_mul_u32_u24_e32 v6, 0x90, v1
	v_and_b32_e32 v7, 0x70, v210
	s_mov_b32 s12, 0x19100
	v_add3_u32 v6, v6, v7, s12
	s_waitcnt vmcnt(7)
	ds_write_b128 v6, v[2:5]

.LBB4_104:
	s_or_b64 exec, exec, s[6:7]
	v_mul_f32_e32 v15, v23, v23
	v_fmac_f32_e32 v15, v22, v22
	v_lshlrev_b32_e32 v20, 1, v219
	s_waitcnt lgkmcnt(0)
	s_barrier
	v_fmac_f32_e32 v15, v24, v24
	s_waitcnt vmcnt(4)
	ds_read_b128 v[6:9], v218
	ds_read_b128 v[16:19], v218 offset:16
	v_lshlrev_b32_e32 v246, 1, v211
	v_xor_b32_e32 v246, v246, v247
	v_add_u32_e32 v20, v246, v20
	v_fmac_f32_e32 v15, v25, v25
	ds_read_b128 v[30:33], v20
	v_fmac_f32_e32 v15, v10, v10
	v_fmac_f32_e32 v15, v11, v11
	v_fmac_f32_e32 v15, v12, v12
	v_fmac_f32_e32 v15, v13, v13
	s_waitcnt lgkmcnt(1)
	v_pk_add_f32 v[12:13], v[12:13], v[18:19]
	v_pk_add_f32 v[10:11], v[10:11], v[16:17]
	ds_read_b128 v[16:19], v20 offset:1280
	v_pk_add_f32 v[8:9], v[24:25], v[8:9]
	v_pk_add_f32 v[6:7], v[22:23], v[6:7]
	v_cvt_pk_f16_f32 v23, v12, v13
	v_cvt_pk_f16_f32 v21, v8, v9
	v_cvt_pk_f16_f32 v22, v10, v11
	v_cvt_pk_f16_f32 v20, v6, v7
	v_add_f32_e32 v5, v5, v15
	ds_write_b128 v220, v[6:9]
	ds_write_b128 v220, v[10:13] offset:16
	s_waitcnt lgkmcnt(3)
	v_mfma_f32_16x16x32_f16 v[0:3], v[30:33], v[20:23], v[0:3]
	s_waitcnt lgkmcnt(2)
	v_mfma_f32_16x16x32_f16 v[6:9], v[16:19], v[20:23], v[26:29]
	ds_read_b128 v[10:13], v221
	ds_read_b128 v[16:19], v223
	ds_read_b128 v[20:23], v223 offset:64
	ds_read_b128 v[24:27], v221 offset:64
	s_waitcnt lgkmcnt(2)
	v_pk_mul_f32 v[10:11], v[16:17], v[10:11]
	s_nop 0
	v_pk_fma_f32 v[0:1], v[0:1], s[4:5], v[10:11] op_sel_hi:[1,0,1]
	v_pk_mul_f32 v[12:13], v[18:19], v[12:13]
	v_pk_mul_f32 v[10:11], v[0:1], v[0:1]
	v_pk_fma_f32 v[2:3], v[2:3], s[4:5], v[12:13] op_sel_hi:[1,0,1]
	v_add_f32_e32 v10, v14, v10
	v_add_f32_e32 v14, v11, v10
	v_pk_mul_f32 v[10:11], v[2:3], v[2:3]
	global_store_dwordx4 v[212:213], v[0:3], off nt
	v_add_f32_e32 v10, v10, v14
	v_add_f32_e32 v10, v11, v10
	s_waitcnt lgkmcnt(0)
	v_pk_mul_f32 v[0:1], v[20:21], v[24:25]
	v_pk_mul_f32 v[2:3], v[22:23], v[26:27]
	v_pk_fma_f32 v[0:1], v[6:7], s[4:5], v[0:1] op_sel_hi:[1,0,1]
	v_pk_fma_f32 v[2:3], v[8:9], s[4:5], v[2:3] op_sel_hi:[1,0,1]
	v_pk_mul_f32 v[6:7], v[0:1], v[0:1]
	global_store_dwordx4 v[212:213], v[0:3], off offset:64 nt
	v_add_f32_e32 v6, v10, v6
	v_add_f32_e32 v10, v7, v6
	v_pk_mul_f32 v[6:7], v[2:3], v[2:3]
	v_mbcnt_lo_u32_b32 v0, -1, 0
	v_add_f32_e32 v6, v6, v10
	v_mbcnt_hi_u32_b32 v2, -1, v0
	v_mov_b32_e32 v0, 0x80
	v_add_f32_e32 v6, v7, v6
	v_lshl_or_b32 v0, v2, 2, v0
	ds_bpermute_b32 v1, v0, v5
	ds_bpermute_b32 v0, v0, v6
	v_and_b32_e32 v3, 63, v2
	v_cmp_gt_u32_e32 vcc, 48, v3
	s_waitcnt lgkmcnt(1)
	v_add_f32_e32 v1, v5, v1
	v_cndmask_b32_e64 v5, 0, 16, vcc
	s_waitcnt lgkmcnt(0)
	v_add_f32_e32 v0, v6, v0
	v_add_lshl_u32 v5, v5, v2, 2
	ds_bpermute_b32 v6, v5, v1
	ds_bpermute_b32 v5, v5, v0
	v_cmp_gt_u32_e32 vcc, 56, v3
	s_waitcnt lgkmcnt(1)
	v_add_f32_e32 v1, v1, v6
	s_waitcnt lgkmcnt(0)
	v_add_f32_e32 v0, v0, v5
	v_cndmask_b32_e64 v5, 0, 8, vcc
	v_add_lshl_u32 v5, v5, v2, 2
	ds_bpermute_b32 v6, v5, v1
	ds_bpermute_b32 v5, v5, v0
	v_cmp_gt_u32_e32 vcc, 60, v3
	s_waitcnt lgkmcnt(1)
	v_add_f32_e32 v1, v1, v6
	s_waitcnt lgkmcnt(0)
	v_add_f32_e32 v0, v0, v5
	v_cndmask_b32_e64 v5, 0, 4, vcc
	v_add_lshl_u32 v5, v5, v2, 2
	ds_bpermute_b32 v6, v5, v1
	ds_bpermute_b32 v5, v5, v0
	v_cmp_gt_u32_e32 vcc, 62, v3
	s_waitcnt lgkmcnt(1)
	v_add_f32_e32 v1, v1, v6
	s_waitcnt lgkmcnt(0)
	v_add_f32_e32 v5, v0, v5
	v_cndmask_b32_e64 v0, 0, 2, vcc
	v_add_lshl_u32 v0, v0, v2, 2
	ds_bpermute_b32 v6, v0, v1
	ds_bpermute_b32 v7, v0, v5
	v_cmp_ne_u32_e32 vcc, 63, v3
	s_waitcnt lgkmcnt(1)
	v_add_f32_e32 v0, v1, v6
	v_addc_co_u32_e32 v2, vcc, 0, v2, vcc
	s_waitcnt lgkmcnt(0)
	v_add_f32_e32 v1, v5, v7
	v_lshlrev_b32_e32 v3, 2, v2
	ds_bpermute_b32 v2, v3, v0
	ds_bpermute_b32 v3, v3, v1
	v_cmp_eq_u32_e32 vcc, 0, v4
	s_and_saveexec_b64 s[2:3], vcc
	s_cbranch_execz .LBB4_106
	s_load_dwordx2 s[0:1], s[0:1], 0x28
	s_lshl_b32 s2, s17, 7
	s_lshl_b32 s3, s16, 1
	s_add_i32 s2, s2, s3
	s_ashr_i32 s3, s2, 31
	s_lshl_b64 s[2:3], s[2:3], 3
	s_waitcnt lgkmcnt(0)
	v_add_f32_e32 v1, v1, v3
	v_add_f32_e32 v0, v0, v2
	s_add_u32 s0, s0, s2
	s_addc_u32 s1, s1, s3
	v_mov_b32_e32 v4, 0
	v_cvt_f64_f32_e32 v[2:3], v0
	v_cvt_f64_f32_e32 v[0:1], v1
	global_store_dwordx4 v4, v[0:3], s[0:1] offset:1024
